# v50 + stick-breaking unmasked arm as scalar f32 ops, arithmetic of the previous key group interleaved under the next group's add/rcp pairs
# speedup vs baseline: 1.0246x; 1.0079x over previous
;     ...
;                     if (diag) { asm volatile("; stick-breaking: diagonal tile (masked)" ::: "memory"); SB_GROUPS(true) } else { SB_GROUPS(false) }
.LBB0_428:
	s_andn2_b64 vcc, exec, s[20:21]
	s_cbranch_vccnz .LBB0_430
	v_add_f32_e32 v25, 1.0, v93
	v_rcp_f32_e32 v25, v25
	v_add_f32_e32 v24, 1.0, v92
	v_rcp_f32_e32 v24, v24
	v_add_f32_e32 v27, 1.0, v91
	v_rcp_f32_e32 v27, v27
	v_add_f32_e32 v26, 1.0, v90
	v_rcp_f32_e32 v26, v26
	v_add_f32_e32 v19, 1.0, v97
	v_rcp_f32_e32 v19, v19
	v_mul_f32_e32 v20, v25, v24
	v_sub_f32_e32 v24, v25, v20
	v_add_f32_e32 v18, 1.0, v95
	v_rcp_f32_e32 v18, v18
	v_mul_f32_e32 v200, v27, v20
	v_sub_f32_e32 v25, v201, v25
	v_add_f32_e32 v23, 1.0, v96
	v_rcp_f32_e32 v23, v23
	v_sub_f32_e32 v27, v20, v200
	v_mul_f32_e32 v20, v26, v200
	v_add_f32_e32 v22, 1.0, v94
	v_rcp_f32_e32 v22, v22
	v_sub_f32_e32 v26, v200, v20
	v_add_f32_e32 v39, 1.0, v79
	v_rcp_f32_e32 v39, v39
	v_mul_f32_e32 v21, v19, v18
	v_sub_f32_e32 v18, v19, v21
	v_add_f32_e32 v38, 1.0, v78
	v_rcp_f32_e32 v38, v38
	v_mul_f32_e32 v45, v23, v21
	v_sub_f32_e32 v19, v201, v19
	v_add_f32_e32 v37, 1.0, v77
	v_rcp_f32_e32 v37, v37
	v_sub_f32_e32 v23, v21, v45
	v_mul_f32_e32 v21, v22, v45
	v_add_f32_e32 v36, 1.0, v76
	v_rcp_f32_e32 v36, v36
	v_sub_f32_e32 v22, v45, v21
	v_add_f32_e32 v29, 1.0, v82
	v_rcp_f32_e32 v29, v29
	v_mul_f32_e32 v32, v39, v38
	v_sub_f32_e32 v38, v39, v32
	v_add_f32_e32 v28, 1.0, v83
	v_rcp_f32_e32 v28, v28
	v_mul_f32_e32 v200, v37, v32
	v_sub_f32_e32 v39, v201, v39
	v_add_f32_e32 v31, 1.0, v81
	v_rcp_f32_e32 v31, v31
	v_sub_f32_e32 v37, v32, v200
	v_mul_f32_e32 v32, v36, v200
	v_add_f32_e32 v30, 1.0, v80
	v_rcp_f32_e32 v30, v30
	v_sub_f32_e32 v36, v200, v32
	v_add_f32_e32 v41, 1.0, v75
	v_rcp_f32_e32 v41, v41
	v_mul_f32_e32 v33, v29, v28
	v_sub_f32_e32 v28, v29, v33
	v_add_f32_e32 v40, 1.0, v74
	v_rcp_f32_e32 v40, v40
	v_mul_f32_e32 v45, v31, v33
	v_sub_f32_e32 v29, v201, v29
	v_add_f32_e32 v43, 1.0, v73
	v_rcp_f32_e32 v43, v43
	v_sub_f32_e32 v31, v33, v45
	v_mul_f32_e32 v33, v30, v45
	v_add_f32_e32 v42, 1.0, v72
	v_rcp_f32_e32 v42, v42
	v_sub_f32_e32 v30, v45, v33
	v_add_f32_e32 v47, 1.0, v71
	v_rcp_f32_e32 v47, v47
	v_mul_f32_e32 v44, v41, v40
	v_sub_f32_e32 v40, v41, v44
	v_add_f32_e32 v46, 1.0, v70
	v_rcp_f32_e32 v46, v46
	v_mul_f32_e32 v200, v43, v44
	v_sub_f32_e32 v41, v201, v41
	v_add_f32_e32 v49, 1.0, v69
	v_rcp_f32_e32 v49, v49
	v_sub_f32_e32 v43, v44, v200
	v_mul_f32_e32 v44, v42, v200
	v_add_f32_e32 v48, 1.0, v68
	v_rcp_f32_e32 v48, v48
	v_sub_f32_e32 v42, v200, v44
	v_add_f32_e32 v61, 1.0, v63
	v_rcp_f32_e32 v61, v61
	v_mul_f32_e32 v50, v47, v46
	v_sub_f32_e32 v46, v47, v50
	v_add_f32_e32 v60, 1.0, v62
	v_rcp_f32_e32 v60, v60
	v_mul_f32_e32 v45, v49, v50
	v_sub_f32_e32 v47, v201, v47
	v_add_f32_e32 v59, 1.0, v34
	v_rcp_f32_e32 v59, v59
	v_sub_f32_e32 v49, v50, v45
	v_mul_f32_e32 v50, v48, v45
	v_add_f32_e32 v58, 1.0, v1
	v_rcp_f32_e32 v58, v58
	v_sub_f32_e32 v48, v45, v50
	v_add_f32_e32 v53, 1.0, v67
	v_rcp_f32_e32 v53, v53
	v_mul_f32_e32 v56, v61, v60
	v_sub_f32_e32 v60, v61, v56
	v_add_f32_e32 v52, 1.0, v66
	v_rcp_f32_e32 v52, v52
	v_mul_f32_e32 v200, v59, v56
	v_sub_f32_e32 v61, v201, v61
	v_add_f32_e32 v55, 1.0, v65
	v_rcp_f32_e32 v55, v55
	v_sub_f32_e32 v59, v56, v200
	v_mul_f32_e32 v56, v58, v200
	v_add_f32_e32 v54, 1.0, v64
	v_rcp_f32_e32 v54, v54
	v_sub_f32_e32 v58, v200, v56
	s_nop 0
	v_mul_f32_e32 v57, v53, v52
	v_sub_f32_e32 v52, v53, v57
	v_mul_f32_e32 v45, v55, v57
	v_sub_f32_e32 v53, v201, v53
	v_sub_f32_e32 v55, v57, v45
	v_mul_f32_e32 v57, v54, v45
	v_sub_f32_e32 v54, v45, v57

;     ...
;                     if (diag) { asm volatile("; stick-breaking: diagonal tile (masked)" ::: "memory"); SB_GROUPS(true) } else { SB_GROUPS(false) }
.LBB0_476:
	s_andn2_b64 vcc, exec, s[30:31]
	s_cbranch_vccnz .LBB0_478
	v_add_f32_e32 v59, 1.0, v151
	v_rcp_f32_e32 v59, v59
	v_add_f32_e32 v58, 1.0, v150
	v_rcp_f32_e32 v58, v58
	v_add_f32_e32 v61, 1.0, v149
	v_rcp_f32_e32 v61, v61
	v_add_f32_e32 v60, 1.0, v131
	v_rcp_f32_e32 v60, v60
	v_add_f32_e32 v53, 1.0, v155
	v_rcp_f32_e32 v53, v53
	v_mul_f32_e32 v54, v59, v58
	v_sub_f32_e32 v58, v59, v54
	v_add_f32_e32 v52, 1.0, v153
	v_rcp_f32_e32 v52, v52
	v_mul_f32_e32 v200, v61, v54
	v_sub_f32_e32 v59, v201, v59
	v_add_f32_e32 v57, 1.0, v154
	v_rcp_f32_e32 v57, v57
	v_sub_f32_e32 v61, v54, v200
	v_mul_f32_e32 v54, v60, v200
	v_add_f32_e32 v56, 1.0, v152
	v_rcp_f32_e32 v56, v56
	v_sub_f32_e32 v60, v200, v54
	v_add_f32_e32 v71, 1.0, v126
	v_rcp_f32_e32 v71, v71
	v_mul_f32_e32 v55, v53, v52
	v_sub_f32_e32 v52, v53, v55
	v_add_f32_e32 v70, 1.0, v125
	v_rcp_f32_e32 v70, v70
	v_mul_f32_e32 v77, v57, v55
	v_sub_f32_e32 v53, v201, v53
	v_add_f32_e32 v69, 1.0, v124
	v_rcp_f32_e32 v69, v69
	v_sub_f32_e32 v57, v55, v77
	v_mul_f32_e32 v55, v56, v77
	v_add_f32_e32 v68, 1.0, v123
	v_rcp_f32_e32 v68, v68
	v_sub_f32_e32 v56, v77, v55
	v_add_f32_e32 v63, 1.0, v129
	v_rcp_f32_e32 v63, v63
	v_mul_f32_e32 v66, v71, v70
	v_sub_f32_e32 v70, v71, v66
	v_add_f32_e32 v62, 1.0, v130
	v_rcp_f32_e32 v62, v62
	v_mul_f32_e32 v200, v69, v66
	v_sub_f32_e32 v71, v201, v71
	v_add_f32_e32 v65, 1.0, v128
	v_rcp_f32_e32 v65, v65
	v_sub_f32_e32 v69, v66, v200
	v_mul_f32_e32 v66, v68, v200
	v_add_f32_e32 v64, 1.0, v127
	v_rcp_f32_e32 v64, v64
	v_sub_f32_e32 v68, v200, v66
	v_add_f32_e32 v73, 1.0, v122
	v_rcp_f32_e32 v73, v73
	v_mul_f32_e32 v67, v63, v62
	v_sub_f32_e32 v62, v63, v67
	v_add_f32_e32 v72, 1.0, v121
	v_rcp_f32_e32 v72, v72
	v_mul_f32_e32 v77, v65, v67
	v_sub_f32_e32 v63, v201, v63
	v_add_f32_e32 v75, 1.0, v120
	v_rcp_f32_e32 v75, v75
	v_sub_f32_e32 v65, v67, v77
	v_mul_f32_e32 v67, v64, v77
	v_add_f32_e32 v74, 1.0, v119
	v_rcp_f32_e32 v74, v74
	v_sub_f32_e32 v64, v77, v67
	v_add_f32_e32 v79, 1.0, v118
	v_rcp_f32_e32 v79, v79
	v_mul_f32_e32 v76, v73, v72
	v_sub_f32_e32 v72, v73, v76
	v_add_f32_e32 v78, 1.0, v117
	v_rcp_f32_e32 v78, v78
	v_mul_f32_e32 v200, v75, v76
	v_sub_f32_e32 v73, v201, v73
	v_add_f32_e32 v81, 1.0, v115
	v_rcp_f32_e32 v81, v81
	v_sub_f32_e32 v75, v76, v200
	v_mul_f32_e32 v76, v74, v200
	v_add_f32_e32 v80, 1.0, v114
	v_rcp_f32_e32 v80, v80
	v_sub_f32_e32 v74, v200, v76
	v_add_f32_e32 v101, 1.0, v109
	v_rcp_f32_e32 v101, v101
	v_mul_f32_e32 v82, v79, v78
	v_sub_f32_e32 v78, v79, v82
	v_add_f32_e32 v100, 1.0, v108
	v_rcp_f32_e32 v100, v100
	v_mul_f32_e32 v77, v81, v82
	v_sub_f32_e32 v79, v201, v79
	v_add_f32_e32 v99, 1.0, v91
	v_rcp_f32_e32 v99, v99
	v_sub_f32_e32 v81, v82, v77
	v_mul_f32_e32 v82, v80, v77
	v_add_f32_e32 v98, 1.0, v34
	v_rcp_f32_e32 v98, v98
	v_sub_f32_e32 v80, v77, v82
	v_add_f32_e32 v93, 1.0, v113
	v_rcp_f32_e32 v93, v93
	v_mul_f32_e32 v96, v101, v100
	v_sub_f32_e32 v100, v101, v96
	v_add_f32_e32 v92, 1.0, v112
	v_rcp_f32_e32 v92, v92
	v_mul_f32_e32 v200, v99, v96
	v_sub_f32_e32 v101, v201, v101
	v_add_f32_e32 v95, 1.0, v111
	v_rcp_f32_e32 v95, v95
	v_sub_f32_e32 v99, v96, v200
	v_mul_f32_e32 v96, v98, v200
	v_add_f32_e32 v94, 1.0, v110
	v_rcp_f32_e32 v94, v94
	v_sub_f32_e32 v98, v200, v96
	s_nop 0
	v_mul_f32_e32 v97, v93, v92
	v_sub_f32_e32 v92, v93, v97
	v_mul_f32_e32 v77, v95, v97
	v_sub_f32_e32 v93, v201, v93
	v_sub_f32_e32 v95, v97, v77
	v_mul_f32_e32 v97, v94, v77
	v_sub_f32_e32 v94, v77, v97
